# PEER V gather A-operand build: scale+range select folded into one SGPR-scaled multiply, one fp8 convert + v_perm byte select instead of zero-init + two converts + and (same operand values)
# speedup vs baseline: 1.0231x; 1.0021x over previous
; __device__ __forceinline__ void peer_unit(Frame& F, const Args& a, int layer, int unit, bool last) {
;     ...
;         f32x2 out[8]; f32x4 hpre[4] = {(f32x4){0.f, 0.f, 0.f, 0.f}, (f32x4){0.f, 0.f, 0.f, 0.f}, (f32x4){0.f, 0.f, 0.f, 0.f}, (f32x4){0.f, 0.f, 0.f, 0.f}}, ac4[4]; v4u gpre[2] = {(v4u){0u, 0u, 0u, 0u}, (v4u){0u, 0u, 0u, 0u}}, p8pre = (v4u){0u, 0u, 0u, 0u}; const bf16* PWG = (const bf16*)(F.ws + WS_PW);
;         const unsigned vmask = ((lane >> 4) == ((lane & 15) >> 2)) ? (0xFFu << (8 * (lane & 3))) : 0u;
.LBB0_1779:
	v_lshrrev_b32_e32 v68, 2, v150
	v_and_b32_e32 v69, 24, v151
	s_movk_i32 s3, 0xff
	v_lshlrev_b32_e64 v69, v69, s3
	v_cmp_eq_u32_e32 vcc, v1, v68
	s_mov_b64 s[6:7], 0x1e00000
	v_lshl_add_u64 v[226:227], v[2:3], 0, s[6:7]
	v_cndmask_b32_e32 v249, 0, v69, vcc
	v_not_b32_e32 v249, v249
	v_and_b32_e32 v249, 0xc0c0c0c, v249
	v_lshlrev_b64 v[2:3], 2, v[224:225]
	v_lshl_add_u64 v[68:69], v[224:225], 1, s[18:19]
	s_mov_b64 s[6:7], 0xe400000
	v_lshl_add_u64 v[228:229], s[20:21], 0, v[2:3]
	v_lshl_add_u64 v[230:231], v[68:69], 0, s[6:7]
	v_lshl_add_u64 v[232:233], s[24:25], 0, v[2:3]
	v_lshl_add_u64 v[2:3], s[18:19], 0, v[224:225]
	s_mov_b64 s[6:7], 0x28400000
	s_mov_b32 s3, 0
	v_lshl_add_u64 v[234:235], v[2:3], 0, s[6:7]
	s_branch .LBB0_1781

.Lpv_skip1:
	s_lshl_b32 s30, s56, 4
	s_cmp_ge_i32 s30, s60
	s_cselect_b64 s[38:39], -1, 0
	s_cmp_lt_i32 s30, s48
	s_cselect_b64 s[52:53], -1, 0
	s_waitcnt lgkmcnt(0)
	s_and_b64 vcc, s[38:39], s[52:53]
	s_cselect_b32 s52, 0x45000000, 0
	v_mul_f32_e32 v1, s52, v170
	v_cvt_pk_fp8_f32 v2, v1, v1
	v_mul_f32_e32 v169, s52, v171
	v_cvt_pk_fp8_f32 v170, v169, v169
	v_mov_b32_e32 v3, v0
	v_perm_b32 v2, v2, v2, v249
	v_mov_b32_e32 v1, v2
	s_nop 0
	v_mfma_f32_16x16x32_fp8_fp8 v[160:163], v[2:3], v[68:69], v[160:163]
	v_mul_f32_e32 v169, s52, v172
	v_mfma_f32_16x16x32_fp8_fp8 v[152:155], v[2:3], v[70:71], v[152:155]
	v_perm_b32 v2, v170, v170, v249
	v_cvt_pk_fp8_f32 v170, v169, v169
	v_mfma_f32_16x16x32_fp8_fp8 v[164:167], v[0:1], v[68:69], v[164:167]
	v_mfma_f32_16x16x32_fp8_fp8 v[156:159], v[0:1], v[70:71], v[156:159]
	v_mov_b32_e32 v1, v2
	v_mfma_f32_16x16x32_fp8_fp8 v[160:163], v[2:3], v[72:73], v[160:163]
	v_mfma_f32_16x16x32_fp8_fp8 v[152:155], v[2:3], v[74:75], v[152:155]
	v_perm_b32 v2, v170, v170, v249
	s_nop 0
	s_nop 0
	v_mfma_f32_16x16x32_fp8_fp8 v[184:187], v[2:3], v[76:77], v[160:163]
	s_nop 1
	s_nop 1
	v_mul_f32_e32 v169, s52, v173
	v_cvt_pk_fp8_f32 v170, v169, v169
	v_mfma_f32_16x16x32_fp8_fp8 v[164:167], v[0:1], v[72:73], v[164:167]
	v_mfma_f32_16x16x32_fp8_fp8 v[156:159], v[0:1], v[74:75], v[156:159]
	v_mov_b32_e32 v1, v2
	v_mfma_f32_16x16x32_fp8_fp8 v[160:163], v[2:3], v[78:79], v[152:155]
	v_perm_b32 v2, v170, v170, v249
	ds_read_b128 v[170:173], v168 offset:16
	v_mfma_f32_16x16x32_fp8_fp8 v[164:167], v[0:1], v[76:77], v[164:167]
	s_waitcnt lgkmcnt(0)
	v_mul_f32_e32 v169, s52, v170
	v_cvt_pk_fp8_f32 v170, v169, v169
	v_mfma_f32_16x16x32_fp8_fp8 v[156:159], v[0:1], v[78:79], v[156:159]
	v_mov_b32_e32 v1, v2
	v_mfma_f32_16x16x32_fp8_fp8 v[152:155], v[2:3], v[80:81], v[184:187]
	v_mul_f32_e32 v169, s52, v171
	v_mfma_f32_16x16x32_fp8_fp8 v[160:163], v[2:3], v[82:83], v[160:163]
	v_perm_b32 v2, v170, v170, v249
	v_cvt_pk_fp8_f32 v170, v169, v169
	v_mfma_f32_16x16x32_fp8_fp8 v[164:167], v[0:1], v[80:81], v[164:167]
	v_mul_f32_e32 v169, s52, v172
	v_mfma_f32_16x16x32_fp8_fp8 v[156:159], v[0:1], v[82:83], v[156:159]
	v_mov_b32_e32 v1, v2
	v_mfma_f32_16x16x32_fp8_fp8 v[152:155], v[2:3], v[84:85], v[152:155]
	v_mfma_f32_16x16x32_fp8_fp8 v[160:163], v[2:3], v[86:87], v[160:163]
	v_perm_b32 v2, v170, v170, v249
	v_cvt_pk_fp8_f32 v170, v169, v169
	v_mfma_f32_16x16x32_fp8_fp8 v[164:167], v[0:1], v[84:85], v[164:167]
	v_mfma_f32_16x16x32_fp8_fp8 v[156:159], v[0:1], v[86:87], v[156:159]
	v_mov_b32_e32 v1, v2
	v_mul_f32_e32 v169, s52, v173
	v_mfma_f32_16x16x32_fp8_fp8 v[152:155], v[2:3], v[88:89], v[152:155]
	v_mfma_f32_16x16x32_fp8_fp8 v[160:163], v[2:3], v[90:91], v[160:163]
	v_perm_b32 v2, v170, v170, v249
	v_cvt_pk_fp8_f32 v170, v169, v169
	v_mfma_f32_16x16x32_fp8_fp8 v[164:167], v[0:1], v[88:89], v[164:167]
	v_mfma_f32_16x16x32_fp8_fp8 v[156:159], v[0:1], v[90:91], v[156:159]
	v_mov_b32_e32 v1, v2
	v_mfma_f32_16x16x32_fp8_fp8 v[152:155], v[2:3], v[92:93], v[152:155]
	v_mfma_f32_16x16x32_fp8_fp8 v[160:163], v[2:3], v[94:95], v[160:163]
	v_perm_b32 v2, v170, v170, v249
	ds_read_b128 v[170:173], v168 offset:32
	s_waitcnt lgkmcnt(0)
	v_mul_f32_e32 v169, s52, v170
	v_cvt_pk_fp8_f32 v170, v169, v169
	v_mfma_f32_16x16x32_fp8_fp8 v[164:167], v[0:1], v[92:93], v[164:167]
	v_mfma_f32_16x16x32_fp8_fp8 v[156:159], v[0:1], v[94:95], v[156:159]
	v_mov_b32_e32 v1, v2
	v_mul_f32_e32 v169, s52, v171
	v_mfma_f32_16x16x32_fp8_fp8 v[152:155], v[2:3], v[96:97], v[152:155]
	v_mfma_f32_16x16x32_fp8_fp8 v[160:163], v[2:3], v[98:99], v[160:163]
	v_perm_b32 v2, v170, v170, v249
	v_cvt_pk_fp8_f32 v170, v169, v169
	v_mfma_f32_16x16x32_fp8_fp8 v[164:167], v[0:1], v[96:97], v[164:167]
	v_mfma_f32_16x16x32_fp8_fp8 v[156:159], v[0:1], v[98:99], v[156:159]
	v_mov_b32_e32 v1, v2
	v_mul_f32_e32 v169, s52, v172
	v_mfma_f32_16x16x32_fp8_fp8 v[152:155], v[2:3], v[100:101], v[152:155]
	v_mfma_f32_16x16x32_fp8_fp8 v[160:163], v[2:3], v[102:103], v[160:163]
	v_perm_b32 v2, v170, v170, v249
	v_cvt_pk_fp8_f32 v170, v169, v169
	v_mfma_f32_16x16x32_fp8_fp8 v[164:167], v[0:1], v[100:101], v[164:167]
	v_mfma_f32_16x16x32_fp8_fp8 v[156:159], v[0:1], v[102:103], v[156:159]
	v_mov_b32_e32 v1, v2
	v_mul_f32_e32 v169, s52, v173
	v_mfma_f32_16x16x32_fp8_fp8 v[152:155], v[2:3], v[104:105], v[152:155]
	v_mfma_f32_16x16x32_fp8_fp8 v[160:163], v[2:3], v[106:107], v[160:163]
	v_perm_b32 v2, v170, v170, v249
	v_cvt_pk_fp8_f32 v170, v169, v169
	v_mfma_f32_16x16x32_fp8_fp8 v[164:167], v[0:1], v[104:105], v[164:167]
	v_mfma_f32_16x16x32_fp8_fp8 v[156:159], v[0:1], v[106:107], v[156:159]
	v_mov_b32_e32 v1, v2
	v_mfma_f32_16x16x32_fp8_fp8 v[152:155], v[2:3], v[108:109], v[152:155]
	v_mfma_f32_16x16x32_fp8_fp8 v[160:163], v[2:3], v[110:111], v[160:163]
	v_perm_b32 v2, v170, v170, v249
	ds_read_b128 v[168:171], v168 offset:48
	v_mfma_f32_16x16x32_fp8_fp8 v[164:167], v[0:1], v[108:109], v[164:167]
	s_waitcnt lgkmcnt(0)
	v_mul_f32_e32 v168, s52, v168
	v_cvt_pk_fp8_f32 v172, v168, v168
	v_mfma_f32_16x16x32_fp8_fp8 v[156:159], v[0:1], v[110:111], v[156:159]
	v_mov_b32_e32 v1, v2
	v_mul_f32_e32 v168, s52, v169
	v_cvt_pk_fp8_f32 v169, v168, v168
	v_mfma_f32_16x16x32_fp8_fp8 v[152:155], v[2:3], v[112:113], v[152:155]
	v_mfma_f32_16x16x32_fp8_fp8 v[160:163], v[2:3], v[114:115], v[160:163]
	v_perm_b32 v2, v172, v172, v249
	v_mfma_f32_16x16x32_fp8_fp8 v[164:167], v[0:1], v[112:113], v[164:167]
	v_mul_f32_e32 v168, s52, v170
	v_mfma_f32_16x16x32_fp8_fp8 v[156:159], v[0:1], v[114:115], v[156:159]
	v_mov_b32_e32 v1, v2
	v_mfma_f32_16x16x32_fp8_fp8 v[152:155], v[2:3], v[120:121], v[152:155]
	s_add_i32 s30, s61, -1
	v_mfma_f32_16x16x32_fp8_fp8 v[160:163], v[2:3], v[122:123], v[160:163]
	v_perm_b32 v2, v169, v169, v249
	v_cvt_pk_fp8_f32 v169, v168, v168
	v_mfma_f32_16x16x32_fp8_fp8 v[164:167], v[0:1], v[120:121], v[164:167]
	s_cmp_lg_u32 s56, s30
	v_mfma_f32_16x16x32_fp8_fp8 v[156:159], v[0:1], v[122:123], v[156:159]
	v_mov_b32_e32 v1, v2
	v_mul_f32_e32 v172, s52, v171
	v_cvt_pk_fp8_f32 v173, v172, v172
	v_mfma_f32_16x16x32_fp8_fp8 v[152:155], v[2:3], v[124:125], v[152:155]
	v_mfma_f32_16x16x32_fp8_fp8 v[160:163], v[2:3], v[126:127], v[160:163]
	v_perm_b32 v2, v169, v169, v249
	v_mfma_f32_16x16x32_fp8_fp8 v[164:167], v[0:1], v[124:125], v[164:167]
	v_mfma_f32_16x16x32_fp8_fp8 v[156:159], v[0:1], v[126:127], v[156:159]
	v_mov_b32_e32 v1, v2
	v_mfma_f32_16x16x32_fp8_fp8 v[152:155], v[2:3], v[144:145], v[152:155]
	v_mfma_f32_16x16x32_fp8_fp8 v[168:171], v[2:3], v[146:147], v[160:163]
	v_perm_b32 v2, v173, v173, v249
	v_mfma_f32_16x16x32_fp8_fp8 v[164:167], v[0:1], v[144:145], v[164:167]
	v_mfma_f32_16x16x32_fp8_fp8 v[156:159], v[0:1], v[146:147], v[156:159]
	v_mov_b32_e32 v1, v2
	s_nop 0
	v_mfma_f32_16x16x32_fp8_fp8 v[160:163], v[2:3], v[148:149], v[152:155]
	v_mfma_f32_16x16x32_fp8_fp8 v[164:167], v[0:1], v[148:149], v[164:167]
	v_mfma_f32_16x16x32_fp8_fp8 v[152:155], v[2:3], v[150:151], v[168:171]
	v_mfma_f32_16x16x32_fp8_fp8 v[156:159], v[0:1], v[150:151], v[156:159]
	s_cbranch_scc1 .LBB0_1816
; __device__ __forceinline__ void peer_token_end(Frame& F, const Args& a, int layer, bool last, bool final_half, size_t tok, int lane, const f32x2 (&out)[8], const f32x4 (&hpre)[4], const v4u (&gpre)[2], const v4u& p8pre) {
;     ...
;     for (int i = 0; i < 4; ++i) { const f32x2 lo = __builtin_amdgcn_cvt_pk_f32_fp8((int)p8pre[i], false), hi = __builtin_amdgcn_cvt_pk_f32_fp8((int)p8pre[i], true);
;         pe[i] = (f32x4){lo.x, lo.y, hi.x, hi.y} * (1.f / 256.f) + (f32x4){out[2 * i].x, out[2 * i].y, out[2 * i + 1].x, out[2 * i + 1].y}; }
;     if (!final_half) {
;         v4u w;
; #pragma unroll
;         for (int i = 0; i < 4; ++i) { const f32x4 s8 = pe[i] * 256.f; int t = 0; t = __builtin_amdgcn_cvt_pk_fp8_f32(s8.x, s8.y, t, false); t = __builtin_amdgcn_cvt_pk_fp8_f32(s8.z, s8.w, t, true); w[i] = (unsigned)t; }
;         *(v4u*)((unsigned char*)(F.ws + WS_P8) + tok * 1024 + 16 * lane) = w;
	v_cvt_pk_f32_fp8_e32 v[2:3], v140
	v_cvt_pk_f32_fp8_e32 v[170:171], v141
	v_cvt_pk_f32_fp8_sdwa v[172:173], v141 src0_sel:WORD_1
	v_cvt_pk_f32_fp8_sdwa v[188:189], v142 src0_sel:WORD_1
	v_pk_mul_f32 v[2:3], v[2:3], s[12:13] op_sel_hi:[1,0]
	v_cvt_pk_f32_fp8_e32 v[186:187], v142
	v_pk_fma_f32 v[174:175], v[160:161], s[14:15], v[2:3] op_sel_hi:[1,0,1]
	v_pk_mul_f32 v[2:3], v[170:171], s[12:13] op_sel_hi:[1,0]
	v_pk_mul_f32 v[170:171], v[172:173], s[12:13] op_sel_hi:[1,0]
	v_cvt_pk_f32_fp8_sdwa v[168:169], v140 src0_sel:WORD_1
	v_pk_fma_f32 v[172:173], v[166:167], s[14:15], v[170:171] op_sel_hi:[1,0,1]
	v_pk_mul_f32 v[170:171], v[188:189], s[12:13] op_sel_hi:[1,0]
	v_cvt_pk_f32_fp8_e32 v[188:189], v143
	v_cvt_pk_f32_fp8_sdwa v[192:193], v143 src0_sel:WORD_1
	s_ashr_i32 s30, s58, 31
	s_add_u32 s52, s0, s58
	v_pk_fma_f32 v[184:185], v[164:165], s[14:15], v[2:3] op_sel_hi:[1,0,1]
	v_pk_mul_f32 v[2:3], v[186:187], s[12:13] op_sel_hi:[1,0]
	s_addc_u32 s53, s1, s30
	v_pk_mul_f32 v[168:169], v[168:169], s[12:13] op_sel_hi:[1,0]
	v_pk_fma_f32 v[186:187], v[154:155], s[14:15], v[170:171] op_sel_hi:[1,0,1]
	v_pk_fma_f32 v[190:191], v[152:153], s[14:15], v[2:3] op_sel_hi:[1,0,1]
	v_pk_mul_f32 v[2:3], v[188:189], s[12:13] op_sel_hi:[1,0]
	v_pk_mul_f32 v[170:171], v[192:193], s[12:13] op_sel_hi:[1,0]
	s_lshl_b64 s[38:39], s[52:53], 10
	v_pk_fma_f32 v[168:169], v[162:163], s[14:15], v[168:169] op_sel_hi:[1,0,1]
	v_pk_fma_f32 v[188:189], v[158:159], s[14:15], v[170:171] op_sel_hi:[1,0,1]
	v_pk_fma_f32 v[192:193], v[156:157], s[14:15], v[2:3] op_sel_hi:[1,0,1]
	s_andn2_b64 vcc, exec, s[46:47]
	s_mov_b64 s[54:55], -1
	s_cbranch_vccnz .LBB0_1811
	v_pk_mul_f32 v[2:3], v[174:175], s[8:9] op_sel_hi:[1,0]
	v_mov_b32_e32 v194, v0
	v_cvt_pk_fp8_f32 v194, v2, v3
	v_pk_mul_f32 v[2:3], v[184:185], s[8:9] op_sel_hi:[1,0]
	v_mov_b32_e32 v195, v0
	v_cvt_pk_fp8_f32 v195, v2, v3
	v_pk_mul_f32 v[2:3], v[168:169], s[8:9] op_sel_hi:[1,0]
	v_mov_b32_e32 v196, v0
	v_cvt_pk_fp8_f32 v194, v2, v3 op_sel:[0,0,1]
	v_pk_mul_f32 v[2:3], v[172:173], s[8:9] op_sel_hi:[1,0]
	v_mov_b32_e32 v197, v0
	v_cvt_pk_fp8_f32 v195, v2, v3 op_sel:[0,0,1]
	v_pk_mul_f32 v[2:3], v[190:191], s[8:9] op_sel_hi:[1,0]
	s_mov_b64 s[54:55], 0
	v_cvt_pk_fp8_f32 v196, v2, v3
	v_pk_mul_f32 v[2:3], v[192:193], s[8:9] op_sel_hi:[1,0]
	s_nop 0
	v_cvt_pk_fp8_f32 v197, v2, v3
	v_pk_mul_f32 v[2:3], v[186:187], s[8:9] op_sel_hi:[1,0]
	s_nop 0
	v_cvt_pk_fp8_f32 v196, v2, v3 op_sel:[0,0,1]
	v_pk_mul_f32 v[2:3], v[188:189], s[8:9] op_sel_hi:[1,0]
	s_nop 0
	v_cvt_pk_fp8_f32 v197, v2, v3 op_sel:[0,0,1]
	v_lshl_add_u64 v[2:3], v[234:235], 0, s[38:39]
	global_store_dwordx4 v[2:3], v[194:197], off

.LBB0_1842:
	s_and_b64 s[38:39], s[6:7], exec
	s_cselect_b32 s52, s61, 0x80
	s_and_b64 s[38:39], s[40:41], exec
	s_cselect_b32 s52, s60, s52
	s_and_b64 s[38:39], s[42:43], exec
	s_cselect_b32 s39, s48, s52
	s_lshl_b32 s52, s57, 9
	s_add_i32 s52, s15, s52
	s_lshl_b32 s53, s59, 6
	s_add_i32 s52, s52, s53
	v_mov_b32_e32 v176, s52
	s_lshr_b32 s38, s39, 4
	s_add_i32 s70, s70, 1
	ds_read_b128 v[178:181], v176
	s_max_u32 s38, s38, s70
	s_lshl_b32 s48, s59, 4
	s_cmp_ge_i32 s48, s30
	s_cselect_b64 s[52:53], -1, 0
	s_cmp_lt_i32 s48, s39
	s_cselect_b64 s[54:55], -1, 0
	s_waitcnt lgkmcnt(0)
	s_and_b64 vcc, s[52:53], s[54:55]
	s_cselect_b32 s54, 0x45000000, 0
	v_mul_f32_e32 v1, s54, v178
	v_cvt_pk_fp8_f32 v2, v1, v1
	v_mul_f32_e32 v177, s54, v179
	v_cvt_pk_fp8_f32 v178, v177, v177
	v_perm_b32 v2, v2, v2, v249
	v_mov_b32_e32 v3, v0
	s_nop 1
	v_mfma_f32_16x16x32_fp8_fp8 v[160:163], v[2:3], v[4:5], v[160:163]
	v_mov_b32_e32 v1, v2
	v_mul_f32_e32 v177, s54, v180
	v_mfma_f32_16x16x32_fp8_fp8 v[152:155], v[2:3], v[6:7], v[152:155]
	v_perm_b32 v2, v178, v178, v249
	v_cvt_pk_fp8_f32 v178, v177, v177
	v_mfma_f32_16x16x32_fp8_fp8 v[164:167], v[0:1], v[4:5], v[164:167]
	v_mfma_f32_16x16x32_fp8_fp8 v[156:159], v[0:1], v[6:7], v[156:159]
	v_mov_b32_e32 v1, v2
	v_mfma_f32_16x16x32_fp8_fp8 v[160:163], v[2:3], v[8:9], v[160:163]
	v_mfma_f32_16x16x32_fp8_fp8 v[152:155], v[2:3], v[10:11], v[152:155]
	v_perm_b32 v2, v178, v178, v249
	s_nop 0
	s_nop 0
	v_mfma_f32_16x16x32_fp8_fp8 v[182:185], v[2:3], v[12:13], v[160:163]
	s_nop 1
	s_nop 1
	v_mul_f32_e32 v177, s54, v181
	v_cvt_pk_fp8_f32 v178, v177, v177
	v_mfma_f32_16x16x32_fp8_fp8 v[164:167], v[0:1], v[8:9], v[164:167]
	v_mfma_f32_16x16x32_fp8_fp8 v[156:159], v[0:1], v[10:11], v[156:159]
	v_mov_b32_e32 v1, v2
	v_mfma_f32_16x16x32_fp8_fp8 v[160:163], v[2:3], v[14:15], v[152:155]
	v_perm_b32 v2, v178, v178, v249
	ds_read_b128 v[178:181], v176 offset:16
	v_mfma_f32_16x16x32_fp8_fp8 v[164:167], v[0:1], v[12:13], v[164:167]
	s_waitcnt lgkmcnt(0)
	v_mul_f32_e32 v177, s54, v178
	v_cvt_pk_fp8_f32 v178, v177, v177
	v_mfma_f32_16x16x32_fp8_fp8 v[156:159], v[0:1], v[14:15], v[156:159]
	v_mov_b32_e32 v1, v2
	v_mfma_f32_16x16x32_fp8_fp8 v[152:155], v[2:3], v[16:17], v[182:185]
	v_mul_f32_e32 v177, s54, v179
	v_mfma_f32_16x16x32_fp8_fp8 v[160:163], v[2:3], v[18:19], v[160:163]
	v_perm_b32 v2, v178, v178, v249
	v_cvt_pk_fp8_f32 v178, v177, v177
	v_mfma_f32_16x16x32_fp8_fp8 v[164:167], v[0:1], v[16:17], v[164:167]
	v_mul_f32_e32 v177, s54, v180
	v_mfma_f32_16x16x32_fp8_fp8 v[156:159], v[0:1], v[18:19], v[156:159]
	v_mov_b32_e32 v1, v2
	v_mfma_f32_16x16x32_fp8_fp8 v[152:155], v[2:3], v[20:21], v[152:155]
	v_mfma_f32_16x16x32_fp8_fp8 v[160:163], v[2:3], v[22:23], v[160:163]
	v_perm_b32 v2, v178, v178, v249
	v_cvt_pk_fp8_f32 v178, v177, v177
	v_mfma_f32_16x16x32_fp8_fp8 v[164:167], v[0:1], v[20:21], v[164:167]
	v_mfma_f32_16x16x32_fp8_fp8 v[156:159], v[0:1], v[22:23], v[156:159]
	v_mov_b32_e32 v1, v2
	v_mul_f32_e32 v177, s54, v181
	v_mfma_f32_16x16x32_fp8_fp8 v[152:155], v[2:3], v[24:25], v[152:155]
	v_mfma_f32_16x16x32_fp8_fp8 v[160:163], v[2:3], v[26:27], v[160:163]
	v_perm_b32 v2, v178, v178, v249
	v_cvt_pk_fp8_f32 v178, v177, v177
	v_mfma_f32_16x16x32_fp8_fp8 v[164:167], v[0:1], v[24:25], v[164:167]
	v_mfma_f32_16x16x32_fp8_fp8 v[156:159], v[0:1], v[26:27], v[156:159]
	v_mov_b32_e32 v1, v2
	v_mfma_f32_16x16x32_fp8_fp8 v[152:155], v[2:3], v[28:29], v[152:155]
	v_mfma_f32_16x16x32_fp8_fp8 v[160:163], v[2:3], v[30:31], v[160:163]
	v_perm_b32 v2, v178, v178, v249
	ds_read_b128 v[178:181], v176 offset:32
	s_waitcnt lgkmcnt(0)
	v_mul_f32_e32 v177, s54, v178
	v_cvt_pk_fp8_f32 v178, v177, v177
	v_mfma_f32_16x16x32_fp8_fp8 v[164:167], v[0:1], v[28:29], v[164:167]
	v_mfma_f32_16x16x32_fp8_fp8 v[156:159], v[0:1], v[30:31], v[156:159]
	v_mov_b32_e32 v1, v2
	v_mul_f32_e32 v177, s54, v179
	v_mfma_f32_16x16x32_fp8_fp8 v[152:155], v[2:3], v[32:33], v[152:155]
	v_mfma_f32_16x16x32_fp8_fp8 v[160:163], v[2:3], v[34:35], v[160:163]
	v_perm_b32 v2, v178, v178, v249
	v_cvt_pk_fp8_f32 v178, v177, v177
	v_mfma_f32_16x16x32_fp8_fp8 v[164:167], v[0:1], v[32:33], v[164:167]
	v_mfma_f32_16x16x32_fp8_fp8 v[156:159], v[0:1], v[34:35], v[156:159]
	v_mov_b32_e32 v1, v2
	v_mul_f32_e32 v177, s54, v180
	v_mfma_f32_16x16x32_fp8_fp8 v[152:155], v[2:3], v[36:37], v[152:155]
	v_mfma_f32_16x16x32_fp8_fp8 v[160:163], v[2:3], v[38:39], v[160:163]
	v_perm_b32 v2, v178, v178, v249
	v_cvt_pk_fp8_f32 v178, v177, v177
	v_mfma_f32_16x16x32_fp8_fp8 v[164:167], v[0:1], v[36:37], v[164:167]
	v_mfma_f32_16x16x32_fp8_fp8 v[156:159], v[0:1], v[38:39], v[156:159]
	v_mov_b32_e32 v1, v2
	v_mul_f32_e32 v177, s54, v181
	v_mfma_f32_16x16x32_fp8_fp8 v[152:155], v[2:3], v[40:41], v[152:155]
	v_mfma_f32_16x16x32_fp8_fp8 v[160:163], v[2:3], v[42:43], v[160:163]
	v_perm_b32 v2, v178, v178, v249
	v_cvt_pk_fp8_f32 v178, v177, v177
	v_mfma_f32_16x16x32_fp8_fp8 v[164:167], v[0:1], v[40:41], v[164:167]
	v_mfma_f32_16x16x32_fp8_fp8 v[156:159], v[0:1], v[42:43], v[156:159]
	v_mov_b32_e32 v1, v2
	v_mfma_f32_16x16x32_fp8_fp8 v[152:155], v[2:3], v[44:45], v[152:155]
	v_mfma_f32_16x16x32_fp8_fp8 v[160:163], v[2:3], v[46:47], v[160:163]
	v_perm_b32 v2, v178, v178, v249
	ds_read_b128 v[176:179], v176 offset:48
	v_mfma_f32_16x16x32_fp8_fp8 v[164:167], v[0:1], v[44:45], v[164:167]
	s_waitcnt lgkmcnt(0)
; __device__ __forceinline__ void peer_token_end(Frame& F, const Args& a, int layer, bool last, bool final_half, size_t tok, int lane, const f32x2 (&out)[8], const f32x4 (&hpre)[4], const v4u (&gpre)[2], const v4u& p8pre) {
;     ...
;     for (int i = 0; i < 4; ++i) { const f32x2 lo = __builtin_amdgcn_cvt_pk_f32_fp8((int)p8pre[i], false), hi = __builtin_amdgcn_cvt_pk_f32_fp8((int)p8pre[i], true);
;         pe[i] = (f32x4){lo.x, lo.y, hi.x, hi.y} * (1.f / 256.f) + (f32x4){out[2 * i].x, out[2 * i].y, out[2 * i + 1].x, out[2 * i + 1].y}; }
;     if (!final_half) {
;         v4u w;
; #pragma unroll
;         for (int i = 0; i < 4; ++i) { const f32x4 s8 = pe[i] * 256.f; int t = 0; t = __builtin_amdgcn_cvt_pk_fp8_f32(s8.x, s8.y, t, false); t = __builtin_amdgcn_cvt_pk_fp8_f32(s8.z, s8.w, t, true); w[i] = (unsigned)t; }
;         *(v4u*)((unsigned char*)(F.ws + WS_P8) + tok * 1024 + 16 * lane) = w;
	v_mul_f32_e32 v176, s54, v176
	v_cvt_pk_fp8_f32 v180, v176, v176
	v_mfma_f32_16x16x32_fp8_fp8 v[156:159], v[0:1], v[46:47], v[156:159]
	v_mov_b32_e32 v1, v2
	v_mul_f32_e32 v176, s54, v177
	v_cvt_pk_fp8_f32 v177, v176, v176
	v_mfma_f32_16x16x32_fp8_fp8 v[152:155], v[2:3], v[48:49], v[152:155]
	v_mfma_f32_16x16x32_fp8_fp8 v[160:163], v[2:3], v[50:51], v[160:163]
	v_perm_b32 v2, v180, v180, v249
	v_mfma_f32_16x16x32_fp8_fp8 v[164:167], v[0:1], v[48:49], v[164:167]
	v_mul_f32_e32 v176, s54, v178
	v_mfma_f32_16x16x32_fp8_fp8 v[156:159], v[0:1], v[50:51], v[156:159]
	v_mov_b32_e32 v1, v2
	v_mfma_f32_16x16x32_fp8_fp8 v[152:155], v[2:3], v[52:53], v[152:155]
	s_add_i32 s38, s38, -1
	v_mfma_f32_16x16x32_fp8_fp8 v[160:163], v[2:3], v[54:55], v[160:163]
	v_perm_b32 v2, v177, v177, v249
	v_cvt_pk_fp8_f32 v177, v176, v176
	v_mfma_f32_16x16x32_fp8_fp8 v[164:167], v[0:1], v[52:53], v[164:167]
	s_cmp_lg_u32 s59, s38
	v_mfma_f32_16x16x32_fp8_fp8 v[156:159], v[0:1], v[54:55], v[156:159]
	v_mov_b32_e32 v1, v2
	v_mul_f32_e32 v180, s54, v179
	v_cvt_pk_fp8_f32 v181, v180, v180
	v_mfma_f32_16x16x32_fp8_fp8 v[152:155], v[2:3], v[56:57], v[152:155]
	v_mfma_f32_16x16x32_fp8_fp8 v[160:163], v[2:3], v[58:59], v[160:163]
	v_perm_b32 v2, v177, v177, v249
	v_mfma_f32_16x16x32_fp8_fp8 v[164:167], v[0:1], v[56:57], v[164:167]
	v_mfma_f32_16x16x32_fp8_fp8 v[156:159], v[0:1], v[58:59], v[156:159]
	v_mov_b32_e32 v1, v2
	v_mfma_f32_16x16x32_fp8_fp8 v[152:155], v[2:3], v[60:61], v[152:155]
	v_mfma_f32_16x16x32_fp8_fp8 v[176:179], v[2:3], v[62:63], v[160:163]
	v_perm_b32 v2, v181, v181, v249
	v_mfma_f32_16x16x32_fp8_fp8 v[164:167], v[0:1], v[60:61], v[164:167]
	v_mfma_f32_16x16x32_fp8_fp8 v[156:159], v[0:1], v[62:63], v[156:159]
	v_mov_b32_e32 v1, v2
	v_mfma_f32_16x16x32_fp8_fp8 v[160:163], v[2:3], v[64:65], v[152:155]
	s_nop 0
	v_mfma_f32_16x16x32_fp8_fp8 v[164:167], v[0:1], v[64:65], v[164:167]
	v_mfma_f32_16x16x32_fp8_fp8 v[152:155], v[2:3], v[66:67], v[176:179]
	v_mfma_f32_16x16x32_fp8_fp8 v[156:159], v[0:1], v[66:67], v[156:159]
	s_cbranch_scc1 .LBB0_1850
	s_waitcnt vmcnt(0)
	v_cvt_pk_f32_fp8_e32 v[2:3], v140
	v_cvt_pk_f32_fp8_e32 v[178:179], v141
	v_cvt_pk_f32_fp8_sdwa v[180:181], v141 src0_sel:WORD_1
	v_cvt_pk_f32_fp8_sdwa v[188:189], v142 src0_sel:WORD_1
	v_pk_mul_f32 v[2:3], v[2:3], s[12:13] op_sel_hi:[1,0]
	v_cvt_pk_f32_fp8_e32 v[186:187], v142
	v_pk_fma_f32 v[182:183], v[160:161], s[14:15], v[2:3] op_sel_hi:[1,0,1]
	v_pk_mul_f32 v[2:3], v[178:179], s[12:13] op_sel_hi:[1,0]
	v_pk_mul_f32 v[178:179], v[180:181], s[12:13] op_sel_hi:[1,0]
	v_cvt_pk_f32_fp8_sdwa v[176:177], v140 src0_sel:WORD_1
	v_pk_fma_f32 v[180:181], v[166:167], s[14:15], v[178:179] op_sel_hi:[1,0,1]
	v_pk_mul_f32 v[178:179], v[188:189], s[12:13] op_sel_hi:[1,0]
	v_cvt_pk_f32_fp8_e32 v[188:189], v143
	v_cvt_pk_f32_fp8_sdwa v[192:193], v143 src0_sel:WORD_1
	s_ashr_i32 s30, s57, 31
	s_add_u32 s52, s0, s57
	v_pk_fma_f32 v[184:185], v[164:165], s[14:15], v[2:3] op_sel_hi:[1,0,1]
	v_pk_mul_f32 v[2:3], v[186:187], s[12:13] op_sel_hi:[1,0]
	s_addc_u32 s53, s1, s30
	v_pk_mul_f32 v[176:177], v[176:177], s[12:13] op_sel_hi:[1,0]
	v_pk_fma_f32 v[186:187], v[154:155], s[14:15], v[178:179] op_sel_hi:[1,0,1]
	v_pk_fma_f32 v[190:191], v[152:153], s[14:15], v[2:3] op_sel_hi:[1,0,1]
	v_pk_mul_f32 v[2:3], v[188:189], s[12:13] op_sel_hi:[1,0]
	v_pk_mul_f32 v[178:179], v[192:193], s[12:13] op_sel_hi:[1,0]
	s_lshl_b64 s[38:39], s[52:53], 10
	v_pk_fma_f32 v[176:177], v[162:163], s[14:15], v[176:177] op_sel_hi:[1,0,1]
	v_pk_fma_f32 v[188:189], v[158:159], s[14:15], v[178:179] op_sel_hi:[1,0,1]
	v_pk_fma_f32 v[192:193], v[156:157], s[14:15], v[2:3] op_sel_hi:[1,0,1]
	s_andn2_b64 vcc, exec, s[46:47]
	s_mov_b64 s[54:55], -1
	s_cbranch_vccnz .LBB0_1845
	v_pk_mul_f32 v[2:3], v[182:183], s[8:9] op_sel_hi:[1,0]
	v_mov_b32_e32 v194, v0
	v_cvt_pk_fp8_f32 v194, v2, v3
	v_pk_mul_f32 v[2:3], v[184:185], s[8:9] op_sel_hi:[1,0]
	v_mov_b32_e32 v195, v0
	v_cvt_pk_fp8_f32 v195, v2, v3
	v_pk_mul_f32 v[2:3], v[176:177], s[8:9] op_sel_hi:[1,0]
	v_mov_b32_e32 v196, v0
	v_cvt_pk_fp8_f32 v194, v2, v3 op_sel:[0,0,1]
	v_pk_mul_f32 v[2:3], v[180:181], s[8:9] op_sel_hi:[1,0]
	v_mov_b32_e32 v197, v0
	v_cvt_pk_fp8_f32 v195, v2, v3 op_sel:[0,0,1]
	v_pk_mul_f32 v[2:3], v[190:191], s[8:9] op_sel_hi:[1,0]
	s_mov_b64 s[54:55], 0
	v_cvt_pk_fp8_f32 v196, v2, v3
	v_pk_mul_f32 v[2:3], v[192:193], s[8:9] op_sel_hi:[1,0]
	s_nop 0
	v_cvt_pk_fp8_f32 v197, v2, v3
	v_pk_mul_f32 v[2:3], v[186:187], s[8:9] op_sel_hi:[1,0]
	s_nop 0
	v_cvt_pk_fp8_f32 v196, v2, v3 op_sel:[0,0,1]
	v_pk_mul_f32 v[2:3], v[188:189], s[8:9] op_sel_hi:[1,0]
	s_nop 0
	v_cvt_pk_fp8_f32 v197, v2, v3 op_sel:[0,0,1]
	v_lshl_add_u64 v[2:3], v[234:235], 0, s[38:39]
	global_store_dwordx4 v[2:3], v[194:197], off
